# branch-merge GEMM epilogue: the 32 gate loads per sub-unit issued back to back with one wait (hipcc had a vmcnt(0) after every load because of the last?wa:load select); on top of v20
# speedup vs baseline: 1.0106x; 1.0075x over previous
.LBB0_1378:
	s_lshl_b32 s6, s26, 8
	s_cmp_eq_u32 s23, 2
	s_cselect_b32 s7, 0x80, 0
	s_add_i32 s6, s6, s60
	v_mbcnt_lo_u32_b32 v134, -1, 0
	v_mbcnt_hi_u32_b32 v134, -1, v134
	s_add_i32 s6, s6, s7
	s_lshl_b32 s4, s4, 8
	v_and_or_b32 v148, v134, 15, s6
	v_ashrrev_i32_e32 v134, 1, v134
	s_or_b32 s4, s4, s61
	v_and_b32_e32 v134, -8, v134
	s_cmp_eq_u32 s5, 1
	s_movk_i32 s23, 0x1300
	v_add_u32_e32 v134, s4, v134
	s_cselect_b32 s4, s23, 0x1700
	s_cmp_eq_u32 s5, 0
	v_mov_b64_e32 v[136:137], s[30:31]
	s_cselect_b32 s4, 0xf00, s4
	v_mad_i64_i32 v[136:137], s[6:7], v148, s88, v[136:137]
	v_add_u32_e32 v220, s4, v134
	s_mov_b64 s[6:7], 0x1e00
	v_ashrrev_i32_e32 v221, 31, v220
	v_lshl_add_u64 v[138:139], v[136:137], 0, s[6:7]
	v_lshl_add_u64 v[136:137], v[138:139], 0, v[220:221]
	global_load_dwordx2 v[218:219], v[136:137], off offset:-3840
	s_cselect_b32 s4, s23, 0x1700
	s_cmp_eq_u32 s5, 2
	v_add_u32_e32 v222, s4, v134
	s_cselect_b64 s[44:45], -1, 0
	s_cmp_lg_u32 s5, 2
	v_ashrrev_i32_e32 v223, 31, v222
	s_cselect_b64 s[6:7], -1, 0
	v_lshl_add_u64 v[138:139], v[138:139], 0, v[222:223]
	global_load_dwordx2 v[216:217], v[138:139], off offset:-3840
	global_load_dwordx2 v[212:213], v[136:137], off offset:-3712
	v_cndmask_b32_e64 v135, 0, 1, s[6:7]
	v_cmp_ne_u32_e64 s[4:5], 1, v135
	global_load_dwordx2 v[210:211], v[138:139], off offset:-3712
	s_waitcnt lgkmcnt(0)
	v_or_b32_e32 v194, 16, v148
	v_mov_b64_e32 v[136:137], s[30:31]
	v_mad_i64_i32 v[136:137], s[6:7], v194, s88, v[136:137]
	s_mov_b64 s[6:7], 0x1e00
	s_nop 0
	v_lshl_add_u64 v[136:137], v[136:137], 0, s[6:7]
	v_lshl_add_u64 v[138:139], v[136:137], 0, v[220:221]
	global_load_dwordx2 v[208:209], v[138:139], off offset:-3840
	v_ashrrev_i32_e32 v149, 31, v148
	v_lshl_add_u64 v[136:137], v[136:137], 0, v[222:223]
	global_load_dwordx2 v[196:197], v[136:137], off offset:-3840
	global_load_dwordx2 v[192:193], v[138:139], off offset:-3712
	global_load_dwordx2 v[190:191], v[136:137], off offset:-3712
	v_or_b32_e32 v184, 32, v148
	v_mov_b64_e32 v[136:137], s[30:31]
	v_mad_i64_i32 v[136:137], s[6:7], v184, s88, v[136:137]
	s_mov_b64 s[6:7], 0x1e00
	s_nop 0
	v_lshl_add_u64 v[136:137], v[136:137], 0, s[6:7]
	v_lshl_add_u64 v[138:139], v[136:137], 0, v[220:221]
	global_load_dwordx2 v[188:189], v[138:139], off offset:-3840
	v_lshl_add_u64 v[136:137], v[136:137], 0, v[222:223]
	global_load_dwordx2 v[186:187], v[136:137], off offset:-3840
	global_load_dwordx2 v[182:183], v[138:139], off offset:-3712
	global_load_dwordx2 v[180:181], v[136:137], off offset:-3712
	v_or_b32_e32 v174, 48, v148
	v_mov_b64_e32 v[136:137], s[30:31]
	v_mad_i64_i32 v[136:137], s[6:7], v174, s88, v[136:137]
	s_mov_b64 s[6:7], 0x1e00
	s_nop 0
	v_lshl_add_u64 v[136:137], v[136:137], 0, s[6:7]
	v_lshl_add_u64 v[138:139], v[136:137], 0, v[220:221]
	global_load_dwordx2 v[178:179], v[138:139], off offset:-3840
	v_lshl_add_u64 v[136:137], v[136:137], 0, v[222:223]
	global_load_dwordx2 v[176:177], v[136:137], off offset:-3840
	global_load_dwordx2 v[172:173], v[138:139], off offset:-3712
	global_load_dwordx2 v[170:171], v[136:137], off offset:-3712
	s_waitcnt vmcnt(0)

.LBB0_1465:
	v_add_u32_e32 v135, 0x80, v148
	v_mov_b64_e32 v[136:137], s[30:31]
	v_mad_i64_i32 v[136:137], s[6:7], v135, s88, v[136:137]
	s_mov_b64 s[6:7], 0x1e00
	s_nop 0
	v_lshl_add_u64 v[136:137], v[136:137], 0, s[6:7]
	v_lshl_add_u64 v[138:139], v[136:137], 0, v[220:221]
	global_load_dwordx2 v[168:169], v[138:139], off offset:-3840
	v_lshl_add_u64 v[136:137], v[136:137], 0, v[222:223]
	global_load_dwordx2 v[166:167], v[136:137], off offset:-3840
	global_load_dwordx2 v[164:165], v[138:139], off offset:-3712
	global_load_dwordx2 v[162:163], v[136:137], off offset:-3712
	v_add_u32_e32 v135, 0x90, v148
	v_mov_b64_e32 v[136:137], s[30:31]
	v_mad_i64_i32 v[136:137], s[6:7], v135, s88, v[136:137]
	s_mov_b64 s[6:7], 0x1e00
	s_nop 0
	v_lshl_add_u64 v[136:137], v[136:137], 0, s[6:7]
	v_lshl_add_u64 v[138:139], v[136:137], 0, v[220:221]
	global_load_dwordx2 v[160:161], v[138:139], off offset:-3840
	v_lshl_add_u64 v[136:137], v[136:137], 0, v[222:223]
	global_load_dwordx2 v[158:159], v[136:137], off offset:-3840
	global_load_dwordx2 v[156:157], v[138:139], off offset:-3712
	global_load_dwordx2 v[154:155], v[136:137], off offset:-3712
	v_add_u32_e32 v135, 0xa0, v148
	v_mov_b64_e32 v[136:137], s[30:31]
	v_mad_i64_i32 v[136:137], s[6:7], v135, s88, v[136:137]
	s_mov_b64 s[6:7], 0x1e00
	s_nop 0
	v_lshl_add_u64 v[136:137], v[136:137], 0, s[6:7]
	v_lshl_add_u64 v[138:139], v[136:137], 0, v[220:221]
	global_load_dwordx2 v[152:153], v[138:139], off offset:-3840
	v_lshl_add_u64 v[136:137], v[136:137], 0, v[222:223]
	global_load_dwordx2 v[150:151], v[136:137], off offset:-3840
	global_load_dwordx2 v[146:147], v[138:139], off offset:-3712
	global_load_dwordx2 v[144:145], v[136:137], off offset:-3712
	v_add_u32_e32 v135, 0xb0, v148
	v_mov_b64_e32 v[136:137], s[30:31]
	v_mad_i64_i32 v[136:137], s[6:7], v135, s88, v[136:137]
	s_mov_b64 s[6:7], 0x1e00
	s_nop 0
	v_lshl_add_u64 v[138:139], v[136:137], 0, s[6:7]
	v_lshl_add_u64 v[136:137], v[138:139], 0, v[220:221]
	global_load_dwordx2 v[142:143], v[136:137], off offset:-3840
	v_lshl_add_u64 v[220:221], v[138:139], 0, v[222:223]
	global_load_dwordx2 v[140:141], v[220:221], off offset:-3840
	global_load_dwordx2 v[138:139], v[136:137], off offset:-3712
	global_load_dwordx2 v[136:137], v[220:221], off offset:-3712
	s_branch .LBB0_1395
